# combo12a + nt on the P6 score stores (134 MB, read once by the next phase)
# speedup vs baseline: 1.0056x; 1.0056x over previous
.LBB0_690:
	s_lshl_b32 s15, s15, 9
	s_lshl_b32 s14, s14, 2
	s_add_i32 s15, s15, s31
	s_add_i32 s14, s15, s14
	v_mbcnt_lo_u32_b32 v160, -1, 0
	v_mbcnt_hi_u32_b32 v160, -1, v160
	v_lshrrev_b32_e32 v161, 5, v160
	v_mul_u32_u24_e32 v162, 0x7c0, v161
	v_sub_u32_e32 v162, 0, v162
	v_ashrrev_i32_e32 v163, 31, v162
	v_sub_u32_e32 v164, 1, v161
	v_mul_u32_u24_e32 v164, 0x7c0, v164
	v_mov_b32_e32 v165, 0
	s_add_i32 s24, s14, 0x0
	s_ashr_i32 s25, s24, 31
	s_lshl_b64 s[24:25], s[24:25], 15
	v_lshl_add_u64 v[166:167], v[132:133], 0, s[24:25]
	v_lshl_add_u64 v[168:169], v[166:167], 0, v[162:163]
	v_lshl_add_u64 v[170:171], v[166:167], 0, v[164:165]
	v_permlane32_swap_b32_e32 v124, v116
	v_permlane32_swap_b32_e32 v125, v117
	v_permlane32_swap_b32_e32 v126, v118
	v_permlane32_swap_b32_e32 v127, v119
	v_permlane32_swap_b32_e32 v108, v100
	v_permlane32_swap_b32_e32 v109, v101
	v_permlane32_swap_b32_e32 v110, v102
	v_permlane32_swap_b32_e32 v111, v103
	s_nop 1
	global_store_dword v[168:169], v124, off offset:0 nt
	global_store_dword v[170:171], v116, off offset:64 nt
	global_store_dword v[168:169], v125, off offset:256 nt
	global_store_dword v[170:171], v117, off offset:320 nt
	global_store_dword v[168:169], v126, off offset:512 nt
	global_store_dword v[170:171], v118, off offset:576 nt
	global_store_dword v[168:169], v127, off offset:768 nt
	global_store_dword v[170:171], v119, off offset:832 nt
	global_store_dword v[168:169], v108, off offset:128 nt
	global_store_dword v[170:171], v100, off offset:192 nt
	global_store_dword v[168:169], v109, off offset:384 nt
	global_store_dword v[170:171], v101, off offset:448 nt
	global_store_dword v[168:169], v110, off offset:640 nt
	global_store_dword v[170:171], v102, off offset:704 nt
	global_store_dword v[168:169], v111, off offset:896 nt
	global_store_dword v[170:171], v103, off offset:960 nt
	s_add_u32 s24, s24, 0x1000
	s_addc_u32 s25, s25, 0
	v_lshl_add_u64 v[166:167], v[132:133], 0, s[24:25]
	v_lshl_add_u64 v[168:169], v[166:167], 0, v[162:163]
	v_lshl_add_u64 v[170:171], v[166:167], 0, v[164:165]
	v_permlane32_swap_b32_e32 v120, v112
	v_permlane32_swap_b32_e32 v121, v113
	v_permlane32_swap_b32_e32 v122, v114
	v_permlane32_swap_b32_e32 v123, v115
	v_permlane32_swap_b32_e32 v104, v96
	v_permlane32_swap_b32_e32 v105, v97
	v_permlane32_swap_b32_e32 v106, v98
	v_permlane32_swap_b32_e32 v107, v99
	s_nop 1
	global_store_dword v[168:169], v120, off offset:0 nt
	global_store_dword v[170:171], v112, off offset:64 nt
	global_store_dword v[168:169], v121, off offset:256 nt
	global_store_dword v[170:171], v113, off offset:320 nt
	global_store_dword v[168:169], v122, off offset:512 nt
	global_store_dword v[170:171], v114, off offset:576 nt
	global_store_dword v[168:169], v123, off offset:768 nt
	global_store_dword v[170:171], v115, off offset:832 nt
	global_store_dword v[168:169], v104, off offset:128 nt
	global_store_dword v[170:171], v96, off offset:192 nt
	global_store_dword v[168:169], v105, off offset:384 nt
	global_store_dword v[170:171], v97, off offset:448 nt
	global_store_dword v[168:169], v106, off offset:640 nt
	global_store_dword v[170:171], v98, off offset:704 nt
	global_store_dword v[168:169], v107, off offset:896 nt
	global_store_dword v[170:171], v99, off offset:960 nt
	s_add_i32 s24, s14, 0x100
	s_ashr_i32 s25, s24, 31
	s_lshl_b64 s[24:25], s[24:25], 15
	v_lshl_add_u64 v[166:167], v[132:133], 0, s[24:25]
	v_lshl_add_u64 v[168:169], v[166:167], 0, v[162:163]
	v_lshl_add_u64 v[170:171], v[166:167], 0, v[164:165]
	v_permlane32_swap_b32_e32 v92, v84
	v_permlane32_swap_b32_e32 v93, v85
	v_permlane32_swap_b32_e32 v94, v86
	v_permlane32_swap_b32_e32 v95, v87
	v_permlane32_swap_b32_e32 v76, v68
	v_permlane32_swap_b32_e32 v77, v69
	v_permlane32_swap_b32_e32 v78, v70
	v_permlane32_swap_b32_e32 v79, v71
	s_nop 1
	global_store_dword v[168:169], v92, off offset:0 nt
	global_store_dword v[170:171], v84, off offset:64 nt
	global_store_dword v[168:169], v93, off offset:256 nt
	global_store_dword v[170:171], v85, off offset:320 nt
	global_store_dword v[168:169], v94, off offset:512 nt
	global_store_dword v[170:171], v86, off offset:576 nt
	global_store_dword v[168:169], v95, off offset:768 nt
	global_store_dword v[170:171], v87, off offset:832 nt
	global_store_dword v[168:169], v76, off offset:128 nt
	global_store_dword v[170:171], v68, off offset:192 nt
	global_store_dword v[168:169], v77, off offset:384 nt
	global_store_dword v[170:171], v69, off offset:448 nt
	global_store_dword v[168:169], v78, off offset:640 nt
	global_store_dword v[170:171], v70, off offset:704 nt
	global_store_dword v[168:169], v79, off offset:896 nt
	global_store_dword v[170:171], v71, off offset:960 nt
	s_add_u32 s24, s24, 0x1000
	s_addc_u32 s25, s25, 0
	v_lshl_add_u64 v[166:167], v[132:133], 0, s[24:25]
	v_lshl_add_u64 v[168:169], v[166:167], 0, v[162:163]
	v_lshl_add_u64 v[170:171], v[166:167], 0, v[164:165]
	v_permlane32_swap_b32_e32 v88, v80
	v_permlane32_swap_b32_e32 v89, v81
	v_permlane32_swap_b32_e32 v90, v82
	v_permlane32_swap_b32_e32 v91, v83
	v_permlane32_swap_b32_e32 v72, v64
	v_permlane32_swap_b32_e32 v73, v65
	v_permlane32_swap_b32_e32 v74, v66
	v_permlane32_swap_b32_e32 v75, v67
	s_nop 1
	global_store_dword v[168:169], v88, off offset:0 nt
	global_store_dword v[170:171], v80, off offset:64 nt
	global_store_dword v[168:169], v89, off offset:256 nt
	global_store_dword v[170:171], v81, off offset:320 nt
	global_store_dword v[168:169], v90, off offset:512 nt
	global_store_dword v[170:171], v82, off offset:576 nt
	global_store_dword v[168:169], v91, off offset:768 nt
	global_store_dword v[170:171], v83, off offset:832 nt
	global_store_dword v[168:169], v72, off offset:128 nt
	global_store_dword v[170:171], v64, off offset:192 nt
	global_store_dword v[168:169], v73, off offset:384 nt
	global_store_dword v[170:171], v65, off offset:448 nt
	global_store_dword v[168:169], v74, off offset:640 nt
	global_store_dword v[170:171], v66, off offset:704 nt
	global_store_dword v[168:169], v75, off offset:896 nt
	global_store_dword v[170:171], v67, off offset:960 nt
	s_add_i32 s24, s14, 0x2
	s_ashr_i32 s25, s24, 31
	s_lshl_b64 s[24:25], s[24:25], 15
	v_lshl_add_u64 v[166:167], v[132:133], 0, s[24:25]
	v_lshl_add_u64 v[168:169], v[166:167], 0, v[162:163]
	v_lshl_add_u64 v[170:171], v[166:167], 0, v[164:165]
	v_permlane32_swap_b32_e32 v60, v52
	v_permlane32_swap_b32_e32 v61, v53
	v_permlane32_swap_b32_e32 v62, v54
	v_permlane32_swap_b32_e32 v63, v55
	v_permlane32_swap_b32_e32 v44, v36
	v_permlane32_swap_b32_e32 v45, v37
	v_permlane32_swap_b32_e32 v46, v38
	v_permlane32_swap_b32_e32 v47, v39
	s_nop 1
	global_store_dword v[168:169], v60, off offset:0 nt
	global_store_dword v[170:171], v52, off offset:64 nt
	global_store_dword v[168:169], v61, off offset:256 nt
	global_store_dword v[170:171], v53, off offset:320 nt
	global_store_dword v[168:169], v62, off offset:512 nt
	global_store_dword v[170:171], v54, off offset:576 nt
	global_store_dword v[168:169], v63, off offset:768 nt
	global_store_dword v[170:171], v55, off offset:832 nt
	global_store_dword v[168:169], v44, off offset:128 nt
	global_store_dword v[170:171], v36, off offset:192 nt
	global_store_dword v[168:169], v45, off offset:384 nt
	global_store_dword v[170:171], v37, off offset:448 nt
	global_store_dword v[168:169], v46, off offset:640 nt
	global_store_dword v[170:171], v38, off offset:704 nt
	global_store_dword v[168:169], v47, off offset:896 nt
	global_store_dword v[170:171], v39, off offset:960 nt
	s_add_u32 s24, s24, 0x1000
	s_addc_u32 s25, s25, 0
	v_lshl_add_u64 v[166:167], v[132:133], 0, s[24:25]
	v_lshl_add_u64 v[168:169], v[166:167], 0, v[162:163]
	v_lshl_add_u64 v[170:171], v[166:167], 0, v[164:165]
	v_permlane32_swap_b32_e32 v56, v48
	v_permlane32_swap_b32_e32 v57, v49
	v_permlane32_swap_b32_e32 v58, v50
	v_permlane32_swap_b32_e32 v59, v51
	v_permlane32_swap_b32_e32 v40, v32
	v_permlane32_swap_b32_e32 v41, v33
	v_permlane32_swap_b32_e32 v42, v34
	v_permlane32_swap_b32_e32 v43, v35
	s_nop 1
	global_store_dword v[168:169], v56, off offset:0 nt
	global_store_dword v[170:171], v48, off offset:64 nt
	global_store_dword v[168:169], v57, off offset:256 nt
	global_store_dword v[170:171], v49, off offset:320 nt
	global_store_dword v[168:169], v58, off offset:512 nt
	global_store_dword v[170:171], v50, off offset:576 nt
	global_store_dword v[168:169], v59, off offset:768 nt
	global_store_dword v[170:171], v51, off offset:832 nt
	global_store_dword v[168:169], v40, off offset:128 nt
	global_store_dword v[170:171], v32, off offset:192 nt
	global_store_dword v[168:169], v41, off offset:384 nt
	global_store_dword v[170:171], v33, off offset:448 nt
	global_store_dword v[168:169], v42, off offset:640 nt
	global_store_dword v[170:171], v34, off offset:704 nt
	global_store_dword v[168:169], v43, off offset:896 nt
	global_store_dword v[170:171], v35, off offset:960 nt
	s_add_i32 s24, s14, 0x102
	s_ashr_i32 s25, s24, 31
	s_lshl_b64 s[24:25], s[24:25], 15
	v_lshl_add_u64 v[166:167], v[132:133], 0, s[24:25]
	v_lshl_add_u64 v[168:169], v[166:167], 0, v[162:163]
	v_lshl_add_u64 v[170:171], v[166:167], 0, v[164:165]
	v_permlane32_swap_b32_e32 v28, v20
	v_permlane32_swap_b32_e32 v29, v21
	v_permlane32_swap_b32_e32 v30, v22
	v_permlane32_swap_b32_e32 v31, v23
	v_permlane32_swap_b32_e32 v12, v4
	v_permlane32_swap_b32_e32 v13, v5
	v_permlane32_swap_b32_e32 v14, v6
	v_permlane32_swap_b32_e32 v15, v7
	s_nop 1
	global_store_dword v[168:169], v28, off offset:0 nt
	global_store_dword v[170:171], v20, off offset:64 nt
	global_store_dword v[168:169], v29, off offset:256 nt
	global_store_dword v[170:171], v21, off offset:320 nt
	global_store_dword v[168:169], v30, off offset:512 nt
	global_store_dword v[170:171], v22, off offset:576 nt
	global_store_dword v[168:169], v31, off offset:768 nt
	global_store_dword v[170:171], v23, off offset:832 nt
	global_store_dword v[168:169], v12, off offset:128 nt
	global_store_dword v[170:171], v4, off offset:192 nt
	global_store_dword v[168:169], v13, off offset:384 nt
	global_store_dword v[170:171], v5, off offset:448 nt
	global_store_dword v[168:169], v14, off offset:640 nt
	global_store_dword v[170:171], v6, off offset:704 nt
	global_store_dword v[168:169], v15, off offset:896 nt
	global_store_dword v[170:171], v7, off offset:960 nt
	s_add_u32 s24, s24, 0x1000
	s_addc_u32 s25, s25, 0
	v_lshl_add_u64 v[166:167], v[132:133], 0, s[24:25]
	v_lshl_add_u64 v[168:169], v[166:167], 0, v[162:163]
	v_lshl_add_u64 v[170:171], v[166:167], 0, v[164:165]
	v_permlane32_swap_b32_e32 v24, v16
	v_permlane32_swap_b32_e32 v25, v17
	v_permlane32_swap_b32_e32 v26, v18
	v_permlane32_swap_b32_e32 v27, v19
	v_permlane32_swap_b32_e32 v8, v0
	v_permlane32_swap_b32_e32 v9, v1
	v_permlane32_swap_b32_e32 v10, v2
	v_permlane32_swap_b32_e32 v11, v3
	s_nop 1
	global_store_dword v[168:169], v24, off offset:0 nt
	global_store_dword v[170:171], v16, off offset:64 nt
	global_store_dword v[168:169], v25, off offset:256 nt
	global_store_dword v[170:171], v17, off offset:320 nt
	global_store_dword v[168:169], v26, off offset:512 nt
	global_store_dword v[170:171], v18, off offset:576 nt
	global_store_dword v[168:169], v27, off offset:768 nt
	global_store_dword v[170:171], v19, off offset:832 nt
	global_store_dword v[168:169], v8, off offset:128 nt
	global_store_dword v[170:171], v0, off offset:192 nt
	global_store_dword v[168:169], v9, off offset:384 nt
	global_store_dword v[170:171], v1, off offset:448 nt
	global_store_dword v[168:169], v10, off offset:640 nt
	global_store_dword v[170:171], v2, off offset:704 nt
	global_store_dword v[168:169], v11, off offset:896 nt
	global_store_dword v[170:171], v3, off offset:960 nt
	s_andn2_b64 vcc, exec, s[4:5]
	s_mov_b64 s[4:5], -1
	s_cbranch_vccnz .LBB0_679
	s_andn2_b64 vcc, exec, s[8:9]
	s_cbranch_vccnz .LBB0_678
	s_barrier
	s_branch .LBB0_678
